# GEMM epilogues: three of the four s_nop 15 pads after the K-loop replaced by s_nop 0 (the first pad plus the barrier already cover the MFMA result latency)
# speedup vs baseline: 1.0055x; 1.0055x over previous
.LBB0_265:
	v_lshl_or_b32 v4, s74, 8, v185
	v_ashrrev_i32_e32 v5, 31, v4
	v_lshl_add_u32 v16, s70, 8, v1
	v_mov_b64_e32 v[2:3], s[24:25]
	v_mad_i64_i32 v[6:7], s[68:69], v16, s67, v[2:3]
	v_lshlrev_b64 v[4:5], 1, v[4:5]
	s_nop 15
	v_lshl_add_u64 v[10:11], v[6:7], 0, v[4:5]
	v_pk_fma_f32 v[6:7], v[158:159], s[16:17], 0 op_sel_hi:[1,0,0]
	s_nop 0
	s_nop 0
	s_nop 0
	v_pk_fma_f32 v[8:9], v[160:161], s[16:17], 0 op_sel_hi:[1,0,0]
	v_cvt_pk_bf16_f32 v6, v6, v7
	v_pk_fma_f32 v[12:13], v[156:157], s[16:17], 0 op_sel_hi:[1,0,0]
	v_cvt_pk_bf16_f32 v7, v8, v9
	v_pk_fma_f32 v[14:15], v[154:155], s[16:17], 0 op_sel_hi:[1,0,0]
	s_andn2_b64 vcc, exec, s[26:27]
	v_cvt_pk_bf16_f32 v8, v14, v15
	v_cvt_pk_bf16_f32 v9, v12, v13
	global_store_dwordx4 v[10:11], v[6:9], off nt
	v_pk_fma_f32 v[12:13], v[144:145], s[16:17], 0 op_sel_hi:[1,0,0]
	v_pk_fma_f32 v[14:15], v[142:143], s[16:17], 0 op_sel_hi:[1,0,0]
	v_pk_fma_f32 v[6:7], v[150:151], s[16:17], 0 op_sel_hi:[1,0,0]
	v_pk_fma_f32 v[8:9], v[152:153], s[16:17], 0 op_sel_hi:[1,0,0]
	v_cvt_pk_bf16_f32 v6, v6, v7
	s_mov_b64 s[26:27], -1
	v_cvt_pk_bf16_f32 v7, v8, v9
	v_cvt_pk_bf16_f32 v8, v14, v15
	v_cvt_pk_bf16_f32 v9, v12, v13
	global_store_dwordx4 v[10:11], v[6:9], off offset:256 nt
	v_pk_fma_f32 v[12:13], v[140:141], s[16:17], 0 op_sel_hi:[1,0,0]
	v_pk_fma_f32 v[14:15], v[138:139], s[16:17], 0 op_sel_hi:[1,0,0]
	v_or_b32_e32 v6, 16, v16
	v_mad_i64_i32 v[6:7], s[68:69], v6, s67, v[2:3]
	v_lshl_add_u64 v[10:11], v[6:7], 0, v[4:5]
	v_pk_fma_f32 v[6:7], v[146:147], s[16:17], 0 op_sel_hi:[1,0,0]
	v_pk_fma_f32 v[8:9], v[148:149], s[16:17], 0 op_sel_hi:[1,0,0]
	v_cvt_pk_bf16_f32 v6, v6, v7
	s_nop 0
	v_cvt_pk_bf16_f32 v7, v8, v9
	v_cvt_pk_bf16_f32 v8, v14, v15
	v_cvt_pk_bf16_f32 v9, v12, v13
	global_store_dwordx4 v[10:11], v[6:9], off nt
	v_pk_fma_f32 v[12:13], v[128:129], s[16:17], 0 op_sel_hi:[1,0,0]
	v_pk_fma_f32 v[14:15], v[126:127], s[16:17], 0 op_sel_hi:[1,0,0]
	v_pk_fma_f32 v[6:7], v[134:135], s[16:17], 0 op_sel_hi:[1,0,0]
	v_pk_fma_f32 v[8:9], v[136:137], s[16:17], 0 op_sel_hi:[1,0,0]
	v_cvt_pk_bf16_f32 v6, v6, v7
	s_nop 0
	v_cvt_pk_bf16_f32 v7, v8, v9
	v_cvt_pk_bf16_f32 v8, v14, v15
	v_cvt_pk_bf16_f32 v9, v12, v13
	global_store_dwordx4 v[10:11], v[6:9], off offset:256 nt
	v_pk_fma_f32 v[12:13], v[124:125], s[16:17], 0 op_sel_hi:[1,0,0]
	v_pk_fma_f32 v[14:15], v[122:123], s[16:17], 0 op_sel_hi:[1,0,0]
	v_or_b32_e32 v6, 32, v16
	v_mad_i64_i32 v[6:7], s[68:69], v6, s67, v[2:3]
	v_lshl_add_u64 v[10:11], v[6:7], 0, v[4:5]
	v_pk_fma_f32 v[6:7], v[130:131], s[16:17], 0 op_sel_hi:[1,0,0]
	v_pk_fma_f32 v[8:9], v[132:133], s[16:17], 0 op_sel_hi:[1,0,0]
	v_cvt_pk_bf16_f32 v6, v6, v7
	s_nop 0
	v_cvt_pk_bf16_f32 v7, v8, v9
	v_cvt_pk_bf16_f32 v8, v14, v15
	v_cvt_pk_bf16_f32 v9, v12, v13
	global_store_dwordx4 v[10:11], v[6:9], off nt
	v_pk_fma_f32 v[12:13], v[112:113], s[16:17], 0 op_sel_hi:[1,0,0]
	v_pk_fma_f32 v[14:15], v[110:111], s[16:17], 0 op_sel_hi:[1,0,0]
	v_pk_fma_f32 v[6:7], v[118:119], s[16:17], 0 op_sel_hi:[1,0,0]
	v_pk_fma_f32 v[8:9], v[120:121], s[16:17], 0 op_sel_hi:[1,0,0]
	v_cvt_pk_bf16_f32 v6, v6, v7
	s_nop 0
	v_cvt_pk_bf16_f32 v7, v8, v9
	v_cvt_pk_bf16_f32 v8, v14, v15
	v_cvt_pk_bf16_f32 v9, v12, v13
	global_store_dwordx4 v[10:11], v[6:9], off offset:256 nt
	v_pk_fma_f32 v[12:13], v[108:109], s[16:17], 0 op_sel_hi:[1,0,0]
	v_pk_fma_f32 v[14:15], v[106:107], s[16:17], 0 op_sel_hi:[1,0,0]
	v_or_b32_e32 v6, 48, v16
	v_mad_i64_i32 v[6:7], s[68:69], v6, s67, v[2:3]
	v_lshl_add_u64 v[10:11], v[6:7], 0, v[4:5]
	v_pk_fma_f32 v[6:7], v[114:115], s[16:17], 0 op_sel_hi:[1,0,0]
	v_pk_fma_f32 v[8:9], v[116:117], s[16:17], 0 op_sel_hi:[1,0,0]
	v_cvt_pk_bf16_f32 v6, v6, v7
	s_nop 0
	v_cvt_pk_bf16_f32 v7, v8, v9
	v_cvt_pk_bf16_f32 v8, v14, v15
	v_cvt_pk_bf16_f32 v9, v12, v13
	global_store_dwordx4 v[10:11], v[6:9], off nt
	v_pk_fma_f32 v[12:13], v[100:101], s[16:17], 0 op_sel_hi:[1,0,0]
	v_pk_fma_f32 v[14:15], v[98:99], s[16:17], 0 op_sel_hi:[1,0,0]
	v_pk_fma_f32 v[6:7], v[102:103], s[16:17], 0 op_sel_hi:[1,0,0]
	v_pk_fma_f32 v[8:9], v[104:105], s[16:17], 0 op_sel_hi:[1,0,0]
	v_cvt_pk_bf16_f32 v6, v6, v7
	s_nop 0
	v_cvt_pk_bf16_f32 v7, v8, v9
	v_cvt_pk_bf16_f32 v8, v14, v15
	v_cvt_pk_bf16_f32 v9, v12, v13
	global_store_dwordx4 v[10:11], v[6:9], off offset:256 nt
	v_pk_fma_f32 v[12:13], v[92:93], s[16:17], 0 op_sel_hi:[1,0,0]
	v_pk_fma_f32 v[14:15], v[90:91], s[16:17], 0 op_sel_hi:[1,0,0]
	v_add_u32_e32 v6, 0x80, v16
	v_mad_i64_i32 v[6:7], s[68:69], v6, s67, v[2:3]
	v_lshl_add_u64 v[10:11], v[6:7], 0, v[4:5]
	v_pk_fma_f32 v[6:7], v[94:95], s[16:17], 0 op_sel_hi:[1,0,0]
	v_pk_fma_f32 v[8:9], v[96:97], s[16:17], 0 op_sel_hi:[1,0,0]
	v_cvt_pk_bf16_f32 v6, v6, v7
	s_nop 0
	v_cvt_pk_bf16_f32 v7, v8, v9
	v_cvt_pk_bf16_f32 v8, v14, v15
	v_cvt_pk_bf16_f32 v9, v12, v13
	global_store_dwordx4 v[10:11], v[6:9], off nt
	v_pk_fma_f32 v[12:13], v[80:81], s[16:17], 0 op_sel_hi:[1,0,0]
	v_pk_fma_f32 v[14:15], v[78:79], s[16:17], 0 op_sel_hi:[1,0,0]
	v_pk_fma_f32 v[6:7], v[86:87], s[16:17], 0 op_sel_hi:[1,0,0]
	v_pk_fma_f32 v[8:9], v[88:89], s[16:17], 0 op_sel_hi:[1,0,0]
	v_cvt_pk_bf16_f32 v6, v6, v7
	s_nop 0
	v_cvt_pk_bf16_f32 v7, v8, v9
	v_cvt_pk_bf16_f32 v8, v14, v15
	v_cvt_pk_bf16_f32 v9, v12, v13
	global_store_dwordx4 v[10:11], v[6:9], off offset:256 nt
	v_pk_fma_f32 v[12:13], v[76:77], s[16:17], 0 op_sel_hi:[1,0,0]
	v_pk_fma_f32 v[14:15], v[74:75], s[16:17], 0 op_sel_hi:[1,0,0]
	v_add_u32_e32 v6, 0x90, v16
	v_mad_i64_i32 v[6:7], s[68:69], v6, s67, v[2:3]
	v_lshl_add_u64 v[10:11], v[6:7], 0, v[4:5]
	v_pk_fma_f32 v[6:7], v[82:83], s[16:17], 0 op_sel_hi:[1,0,0]
	v_pk_fma_f32 v[8:9], v[84:85], s[16:17], 0 op_sel_hi:[1,0,0]
	v_cvt_pk_bf16_f32 v6, v6, v7
	s_nop 0
	v_cvt_pk_bf16_f32 v7, v8, v9
	v_cvt_pk_bf16_f32 v8, v14, v15
	v_cvt_pk_bf16_f32 v9, v12, v13
	global_store_dwordx4 v[10:11], v[6:9], off nt
	v_pk_fma_f32 v[12:13], v[64:65], s[16:17], 0 op_sel_hi:[1,0,0]
	v_pk_fma_f32 v[14:15], v[62:63], s[16:17], 0 op_sel_hi:[1,0,0]
	v_pk_fma_f32 v[6:7], v[70:71], s[16:17], 0 op_sel_hi:[1,0,0]
	v_pk_fma_f32 v[8:9], v[72:73], s[16:17], 0 op_sel_hi:[1,0,0]
	v_cvt_pk_bf16_f32 v6, v6, v7
	s_nop 0
	v_cvt_pk_bf16_f32 v7, v8, v9
	v_cvt_pk_bf16_f32 v8, v14, v15
	v_cvt_pk_bf16_f32 v9, v12, v13
	global_store_dwordx4 v[10:11], v[6:9], off offset:256 nt
	v_pk_fma_f32 v[12:13], v[60:61], s[16:17], 0 op_sel_hi:[1,0,0]
	v_pk_fma_f32 v[14:15], v[58:59], s[16:17], 0 op_sel_hi:[1,0,0]
	v_add_u32_e32 v6, 0xa0, v16
	v_mad_i64_i32 v[6:7], s[68:69], v6, s67, v[2:3]
	v_lshl_add_u64 v[10:11], v[6:7], 0, v[4:5]
	v_pk_fma_f32 v[6:7], v[66:67], s[16:17], 0 op_sel_hi:[1,0,0]
	v_pk_fma_f32 v[8:9], v[68:69], s[16:17], 0 op_sel_hi:[1,0,0]
	v_cvt_pk_bf16_f32 v6, v6, v7
	s_nop 0
	v_cvt_pk_bf16_f32 v7, v8, v9
	v_cvt_pk_bf16_f32 v8, v14, v15
	v_cvt_pk_bf16_f32 v9, v12, v13
	global_store_dwordx4 v[10:11], v[6:9], off nt
	v_pk_fma_f32 v[12:13], v[48:49], s[16:17], 0 op_sel_hi:[1,0,0]
	v_pk_fma_f32 v[14:15], v[46:47], s[16:17], 0 op_sel_hi:[1,0,0]
	v_pk_fma_f32 v[6:7], v[54:55], s[16:17], 0 op_sel_hi:[1,0,0]
	v_pk_fma_f32 v[8:9], v[56:57], s[16:17], 0 op_sel_hi:[1,0,0]
	v_cvt_pk_bf16_f32 v6, v6, v7
	s_nop 0
	v_cvt_pk_bf16_f32 v7, v8, v9
	v_cvt_pk_bf16_f32 v8, v14, v15
	v_cvt_pk_bf16_f32 v9, v12, v13
	global_store_dwordx4 v[10:11], v[6:9], off offset:256 nt
	v_pk_fma_f32 v[10:11], v[42:43], s[16:17], 0 op_sel_hi:[1,0,0]
	s_nop 0
	v_add_u32_e32 v6, 0xb0, v16
	v_mad_i64_i32 v[2:3], s[68:69], v6, s67, v[2:3]
	v_lshl_add_u64 v[6:7], v[2:3], 0, v[4:5]
	v_pk_fma_f32 v[4:5], v[52:53], s[16:17], 0 op_sel_hi:[1,0,0]
	v_pk_fma_f32 v[2:3], v[50:51], s[16:17], 0 op_sel_hi:[1,0,0]
	v_pk_fma_f32 v[8:9], v[44:45], s[16:17], 0 op_sel_hi:[1,0,0]
	v_cvt_pk_bf16_f32 v2, v2, v3
	v_cvt_pk_bf16_f32 v3, v4, v5
	v_cvt_pk_bf16_f32 v4, v10, v11
	v_pk_fma_f32 v[10:11], v[34:35], s[16:17], 0 op_sel_hi:[1,0,0]
	v_cvt_pk_bf16_f32 v5, v8, v9
	global_store_dwordx4 v[6:7], v[2:5], off nt
	v_pk_fma_f32 v[8:9], v[36:37], s[16:17], 0 op_sel_hi:[1,0,0]
	s_nop 0
	v_pk_fma_f32 v[4:5], v[40:41], s[16:17], 0 op_sel_hi:[1,0,0]
	v_pk_fma_f32 v[2:3], v[38:39], s[16:17], 0 op_sel_hi:[1,0,0]
	s_nop 0
	v_cvt_pk_bf16_f32 v2, v2, v3
	v_cvt_pk_bf16_f32 v3, v4, v5
	v_cvt_pk_bf16_f32 v4, v10, v11
	v_cvt_pk_bf16_f32 v5, v8, v9
	global_store_dwordx4 v[6:7], v[2:5], off offset:256 nt
	s_cbranch_vccnz .LBB0_250
	s_andn2_b64 vcc, exec, s[6:7]
	s_cbranch_vccnz .LBB0_249
	s_barrier
	s_branch .LBB0_249

.LBB0_1203:
	s_lshr_b64 s[54:55], s[52:53], 24
	s_and_b32 s1, s54, 0xffffff00
	v_lshl_add_u32 v4, s52, 8, v1
	v_or_b32_e32 v2, s1, v179
	v_mad_i64_i32 v[10:11], s[52:53], v4, s73, 0
	v_lshl_add_u64 v[6:7], v[10:11], 1, s[12:13]
	v_ashrrev_i32_e32 v3, 31, v2
	v_lshl_add_u64 v[8:9], v[2:3], 1, v[6:7]
	s_nop 15
	s_nop 0
	s_nop 0
	s_nop 0
	v_mad_i64_i32 v[254:255], s[98:99], v4, s73, 0
	v_lshl_add_u64 v[254:255], v[254:255], 1, s[12:13]
	v_lshl_add_u64 v[254:255], v[2:3], 1, v[254:255]
	global_load_dwordx4 v[196:199], v[254:255], off
	global_load_dwordx4 v[200:203], v[254:255], off offset:256
	v_or_b32_e32 v254, 16, v4
	v_mad_i64_i32 v[254:255], s[98:99], v254, s73, 0
	v_lshl_add_u64 v[254:255], v[254:255], 1, s[12:13]
	v_lshl_add_u64 v[254:255], v[2:3], 1, v[254:255]
	global_load_dwordx4 v[204:207], v[254:255], off
	global_load_dwordx4 v[208:211], v[254:255], off offset:256
	v_or_b32_e32 v254, 32, v4
	v_mad_i64_i32 v[254:255], s[98:99], v254, s73, 0
	v_lshl_add_u64 v[254:255], v[254:255], 1, s[12:13]
	v_lshl_add_u64 v[254:255], v[2:3], 1, v[254:255]
	global_load_dwordx4 v[212:215], v[254:255], off
	global_load_dwordx4 v[216:219], v[254:255], off offset:256
	v_or_b32_e32 v254, 48, v4
	v_mad_i64_i32 v[254:255], s[98:99], v254, s73, 0
	v_lshl_add_u64 v[254:255], v[254:255], 1, s[12:13]
	v_lshl_add_u64 v[254:255], v[2:3], 1, v[254:255]
	global_load_dwordx4 v[220:223], v[254:255], off
	global_load_dwordx4 v[224:227], v[254:255], off offset:256
	v_add_u32_e32 v254, 0x80, v4
	v_mad_i64_i32 v[254:255], s[98:99], v254, s73, 0
	v_lshl_add_u64 v[254:255], v[254:255], 1, s[12:13]
	v_lshl_add_u64 v[254:255], v[2:3], 1, v[254:255]
	global_load_dwordx4 v[182:185], v[254:255], off
	global_load_dwordx4 v[186:189], v[254:255], off offset:256
	v_add_u32_e32 v254, 0x90, v4
	v_mad_i64_i32 v[254:255], s[98:99], v254, s73, 0
	v_lshl_add_u64 v[254:255], v[254:255], 1, s[12:13]
	v_lshl_add_u64 v[254:255], v[2:3], 1, v[254:255]
	global_load_dwordx4 v[238:241], v[254:255], off
	global_load_dwordx4 v[242:245], v[254:255], off offset:256
	v_add_u32_e32 v254, 0xa0, v4
	v_mad_i64_i32 v[254:255], s[98:99], v254, s73, 0
	v_lshl_add_u64 v[254:255], v[254:255], 1, s[12:13]
	v_lshl_add_u64 v[254:255], v[2:3], 1, v[254:255]
	global_load_dwordx4 v[246:249], v[254:255], off
	global_load_dwordx4 v[250:253], v[254:255], off offset:256
	v_ashrrev_i32_e32 v5, 31, v4
	v_lshlrev_b64 v[6:7], 11, v[4:5]
	s_cmp_lg_u32 s0, 0
	v_lshl_add_u64 v[6:7], s[4:5], 0, v[6:7]
	s_cselect_b64 s[52:53], -1, 0
	s_cmp_eq_u32 s0, 0
	v_lshl_add_u64 v[6:7], v[6:7], 0, v[2:3]
	s_waitcnt vmcnt(0)
	v_lshlrev_b32_e32 v18, 16, v196
	v_and_b32_e32 v17, 0xffff0000, v196
	v_lshlrev_b32_e32 v16, 16, v197
	v_and_b32_e32 v15, 0xffff0000, v197
	v_lshlrev_b32_e32 v14, 16, v198
	v_and_b32_e32 v13, 0xffff0000, v198
	v_lshlrev_b32_e32 v12, 16, v199
	v_and_b32_e32 v5, 0xffff0000, v199
	s_cbranch_scc1 .LBB0_1256
	v_mul_f32_e32 v19, 0xbfb8aa3b, v18
	v_mul_f32_e32 v20, 0xbfb8aa3b, v17
	v_exp_f32_e32 v19, v19
	v_mul_f32_e32 v21, 0xbfb8aa3b, v16
	v_exp_f32_e32 v20, v20
	v_mul_f32_e32 v23, 0xbfb8aa3b, v14
	v_mul_f32_e32 v24, 0xbfb8aa3b, v13
	v_exp_f32_e32 v21, v21
	v_exp_f32_e32 v23, v23
	v_exp_f32_e32 v24, v24
	v_mul_f32_e32 v22, 0xbfb8aa3b, v15
	v_add_f32_e32 v19, 1.0, v19
	v_add_f32_e32 v20, 1.0, v20
	v_exp_f32_e32 v22, v22
	v_mul_f32_e32 v25, 0xbfb8aa3b, v12
	v_mul_f32_e32 v27, 0xbfb8aa3b, v5
	v_rcp_f32_e32 v19, v19
	v_rcp_f32_e32 v20, v20
	v_add_f32_e32 v21, 1.0, v21
	v_add_f32_e32 v23, 1.0, v23
	v_add_f32_e32 v24, 1.0, v24
	v_exp_f32_e32 v25, v25
	v_exp_f32_e32 v27, v27
	v_rcp_f32_e32 v21, v21
	v_rcp_f32_e32 v23, v23
	v_rcp_f32_e32 v24, v24
	v_add_f32_e32 v22, 1.0, v22
	v_mul_f32_e32 v19, v154, v19
	v_mul_f32_e32 v20, v155, v20
	v_rcp_f32_e32 v22, v22
	v_add_f32_e32 v25, 1.0, v25
	v_add_f32_e32 v27, 1.0, v27
	v_mul_f32_e32 v21, v156, v21
	v_rcp_f32_e32 v25, v25
	v_rcp_f32_e32 v27, v27
	v_mul_f32_e32 v23, v150, v23
	v_mul_f32_e32 v24, v151, v24
	v_mul_f32_e32 v19, 0x3c000000, v19
	v_mul_f32_e32 v28, 0x3c000000, v20
	v_mov_b32_e32 v20, 0
	v_mul_f32_e32 v29, 0x3c000000, v21
	v_cvt_pk_fp8_f32 v20, v19, v28
	v_mul_f32_e32 v19, 0x3c000000, v23
	v_mul_f32_e32 v23, 0x3c000000, v24
	v_mov_b32_e32 v21, 0
	v_cvt_pk_fp8_f32 v21, v19, v23
	v_mul_f32_e32 v22, v157, v22
	v_mul_f32_e32 v25, v152, v25
	v_mul_f32_e32 v27, v153, v27
	v_mul_f32_e32 v22, 0x3c000000, v22
	v_cvt_pk_fp8_f32 v20, v29, v22 op_sel:[0,0,1]
	v_mul_f32_e32 v19, 0x3c000000, v25
	v_mul_f32_e32 v22, 0x3c000000, v27
	v_cvt_pk_fp8_f32 v21, v19, v22 op_sel:[0,0,1]
	global_store_dwordx2 v[6:7], v[20:21], off
	v_lshl_add_u64 v[10:11], v[10:11], 1, s[10:11]
	s_cbranch_execnz .LBB0_1206

.LBB0_1348:
	v_lshl_or_b32 v18, s74, 8, v185
	v_ashrrev_i32_e32 v19, 31, v18
	v_lshl_add_u64 v[2:3], v[18:19], 2, s[8:9]
	s_nop 15
	s_nop 0
	s_nop 0
	s_nop 0
	global_load_dwordx4 v[14:17], v[2:3], off
	global_load_dwordx4 v[10:13], v[2:3], off offset:16
	global_load_dwordx4 v[6:9], v[2:3], off offset:512
	s_nop 0
	global_load_dwordx4 v[2:5], v[2:3], off offset:528
	v_lshl_add_u32 v24, s60, 8, v1
	v_ashrrev_i32_e32 v25, 31, v24
	v_pk_mul_f32 v[20:21], v[160:161], s[14:15] op_sel_hi:[1,0]
	v_pk_mul_f32 v[22:23], v[158:159], s[14:15] op_sel_hi:[1,0]
	v_pk_mul_f32 v[28:29], v[154:155], s[14:15] op_sel_hi:[1,0]
	v_pk_mul_f32 v[32:33], v[150:151], s[14:15] op_sel_hi:[1,0]
	v_or_b32_e32 v150, 16, v24
	v_lshlrev_b64 v[154:155], 12, v[24:25]
	v_pk_mul_f32 v[26:27], v[156:157], s[14:15] op_sel_hi:[1,0]
	v_lshlrev_b64 v[156:157], 1, v[18:19]
	v_ashrrev_i32_e32 v151, 31, v150
	v_lshl_add_u64 v[18:19], s[42:43], 0, v[154:155]
	v_pk_mul_f32 v[30:31], v[152:153], s[14:15] op_sel_hi:[1,0]
	v_pk_mul_f32 v[148:149], v[148:149], s[14:15] op_sel_hi:[1,0]
	v_pk_mul_f32 v[146:147], v[146:147], s[14:15] op_sel_hi:[1,0]
	v_or_b32_e32 v152, 32, v24
	v_lshlrev_b64 v[150:151], 12, v[150:151]
	v_lshl_add_u64 v[18:19], v[18:19], 0, v[156:157]
	v_pk_mul_f32 v[144:145], v[144:145], s[14:15] op_sel_hi:[1,0]
	v_pk_mul_f32 v[142:143], v[142:143], s[14:15] op_sel_hi:[1,0]
	v_pk_mul_f32 v[140:141], v[140:141], s[14:15] op_sel_hi:[1,0]
	v_pk_mul_f32 v[138:139], v[138:139], s[14:15] op_sel_hi:[1,0]
	v_ashrrev_i32_e32 v153, 31, v152
	v_lshl_add_u64 v[150:151], s[42:43], 0, v[150:151]
	v_pk_mul_f32 v[136:137], v[136:137], s[14:15] op_sel_hi:[1,0]
	v_pk_mul_f32 v[134:135], v[134:135], s[14:15] op_sel_hi:[1,0]
	v_pk_mul_f32 v[132:133], v[132:133], s[14:15] op_sel_hi:[1,0]
	v_pk_mul_f32 v[130:131], v[130:131], s[14:15] op_sel_hi:[1,0]
	v_lshlrev_b64 v[152:153], 12, v[152:153]
	v_lshl_add_u64 v[150:151], v[150:151], 0, v[156:157]
	v_pk_mul_f32 v[128:129], v[128:129], s[14:15] op_sel_hi:[1,0]
	v_pk_mul_f32 v[126:127], v[126:127], s[14:15] op_sel_hi:[1,0]
	v_pk_mul_f32 v[124:125], v[124:125], s[14:15] op_sel_hi:[1,0]
	v_pk_mul_f32 v[122:123], v[122:123], s[14:15] op_sel_hi:[1,0]
	v_lshl_add_u64 v[152:153], s[42:43], 0, v[152:153]
	v_lshl_add_u64 v[152:153], v[152:153], 0, v[156:157]
	s_waitcnt vmcnt(0)
	v_pk_mul_f32 v[154:155], v[20:21], v[16:17]
	v_pk_mul_f32 v[20:21], v[22:23], v[14:15]
	v_pk_mul_f32 v[22:23], v[28:29], v[10:11]
	v_pk_mul_f32 v[26:27], v[26:27], v[12:13]
	v_cvt_pk_bf16_f32 v20, v20, v21
	v_cvt_pk_bf16_f32 v21, v154, v155
	v_cvt_pk_bf16_f32 v22, v22, v23
	v_pk_mul_f32 v[28:29], v[30:31], v[8:9]
	v_cvt_pk_bf16_f32 v23, v26, v27
	v_pk_mul_f32 v[30:31], v[32:33], v[6:7]
	v_pk_mul_f32 v[32:33], v[148:149], v[4:5]
	v_pk_mul_f32 v[146:147], v[146:147], v[2:3]
	global_store_dwordx4 v[18:19], v[20:23], off
	v_pk_mul_f32 v[144:145], v[144:145], v[16:17]
	v_pk_mul_f32 v[142:143], v[142:143], v[14:15]
	v_cvt_pk_bf16_f32 v20, v30, v31
	v_cvt_pk_bf16_f32 v21, v28, v29
	v_cvt_pk_bf16_f32 v22, v146, v147
	v_cvt_pk_bf16_f32 v23, v32, v33
	v_pk_mul_f32 v[140:141], v[140:141], v[12:13]
	v_pk_mul_f32 v[138:139], v[138:139], v[10:11]
	global_store_dwordx4 v[18:19], v[20:23], off offset:256
	v_pk_mul_f32 v[136:137], v[136:137], v[8:9]
	v_pk_mul_f32 v[134:135], v[134:135], v[6:7]
	v_cvt_pk_bf16_f32 v20, v142, v143
	v_cvt_pk_bf16_f32 v21, v144, v145
	v_cvt_pk_bf16_f32 v22, v138, v139
	v_cvt_pk_bf16_f32 v23, v140, v141
	v_pk_mul_f32 v[132:133], v[132:133], v[4:5]
	v_pk_mul_f32 v[130:131], v[130:131], v[2:3]
	global_store_dwordx4 v[150:151], v[20:23], off
	v_pk_mul_f32 v[128:129], v[128:129], v[16:17]
	v_pk_mul_f32 v[126:127], v[126:127], v[14:15]
	v_cvt_pk_bf16_f32 v20, v134, v135
	v_cvt_pk_bf16_f32 v21, v136, v137
	v_cvt_pk_bf16_f32 v22, v130, v131
	v_cvt_pk_bf16_f32 v23, v132, v133
	v_pk_mul_f32 v[124:125], v[124:125], v[12:13]
	v_pk_mul_f32 v[122:123], v[122:123], v[10:11]
	global_store_dwordx4 v[150:151], v[20:23], off offset:256
	v_pk_mul_f32 v[28:29], v[114:115], s[14:15] op_sel_hi:[1,0]
	s_nop 0
	v_cvt_pk_bf16_f32 v20, v126, v127
	v_cvt_pk_bf16_f32 v21, v128, v129
	v_cvt_pk_bf16_f32 v22, v122, v123
	v_cvt_pk_bf16_f32 v23, v124, v125
	global_store_dwordx4 v[152:153], v[20:23], off
	s_nop 1
	v_pk_mul_f32 v[20:21], v[120:121], s[14:15] op_sel_hi:[1,0]
	v_pk_mul_f32 v[22:23], v[118:119], s[14:15] op_sel_hi:[1,0]
	v_pk_mul_f32 v[26:27], v[20:21], v[8:9]
	v_pk_mul_f32 v[20:21], v[22:23], v[6:7]
	v_pk_mul_f32 v[22:23], v[116:117], s[14:15] op_sel_hi:[1,0]
	v_cvt_pk_bf16_f32 v20, v20, v21
	v_cvt_pk_bf16_f32 v21, v26, v27
	s_nop 0
	v_pk_mul_f32 v[30:31], v[22:23], v[4:5]
	v_pk_mul_f32 v[22:23], v[28:29], v[2:3]
	v_pk_mul_f32 v[28:29], v[106:107], s[14:15] op_sel_hi:[1,0]
	v_cvt_pk_bf16_f32 v22, v22, v23
	v_cvt_pk_bf16_f32 v23, v30, v31
	global_store_dwordx4 v[152:153], v[20:23], off offset:256
	s_nop 1
	v_or_b32_e32 v20, 48, v24
	v_ashrrev_i32_e32 v21, 31, v20
	v_lshlrev_b64 v[20:21], 12, v[20:21]
	v_lshl_add_u64 v[20:21], s[42:43], 0, v[20:21]
	v_lshl_add_u64 v[24:25], v[20:21], 0, v[156:157]
	v_pk_mul_f32 v[20:21], v[112:113], s[14:15] op_sel_hi:[1,0]
	v_pk_mul_f32 v[22:23], v[110:111], s[14:15] op_sel_hi:[1,0]
	v_pk_mul_f32 v[26:27], v[20:21], v[16:17]
	v_pk_mul_f32 v[20:21], v[22:23], v[14:15]
	v_pk_mul_f32 v[22:23], v[108:109], s[14:15] op_sel_hi:[1,0]
	v_cvt_pk_bf16_f32 v20, v20, v21
	v_cvt_pk_bf16_f32 v21, v26, v27
	s_nop 0
	v_pk_mul_f32 v[30:31], v[22:23], v[12:13]
	v_pk_mul_f32 v[22:23], v[28:29], v[10:11]
	v_pk_mul_f32 v[28:29], v[98:99], s[14:15] op_sel_hi:[1,0]
	v_cvt_pk_bf16_f32 v22, v22, v23
	v_cvt_pk_bf16_f32 v23, v30, v31
	global_store_dwordx4 v[24:25], v[20:23], off
	s_nop 1
	v_pk_mul_f32 v[20:21], v[104:105], s[14:15] op_sel_hi:[1,0]
	v_pk_mul_f32 v[22:23], v[102:103], s[14:15] op_sel_hi:[1,0]
	v_pk_mul_f32 v[26:27], v[20:21], v[8:9]
	v_pk_mul_f32 v[20:21], v[22:23], v[6:7]
	v_pk_mul_f32 v[22:23], v[100:101], s[14:15] op_sel_hi:[1,0]
	v_cvt_pk_bf16_f32 v20, v20, v21
	v_cvt_pk_bf16_f32 v21, v26, v27
	s_nop 0
	v_pk_mul_f32 v[30:31], v[22:23], v[4:5]
	v_pk_mul_f32 v[22:23], v[28:29], v[2:3]
	v_pk_mul_f32 v[28:29], v[90:91], s[14:15] op_sel_hi:[1,0]
	v_cvt_pk_bf16_f32 v22, v22, v23
	v_cvt_pk_bf16_f32 v23, v30, v31
	global_store_dwordx4 v[24:25], v[20:23], off offset:256
	v_lshl_add_u64 v[24:25], v[18:19], 0, s[16:17]
	s_nop 0
	v_pk_mul_f32 v[20:21], v[96:97], s[14:15] op_sel_hi:[1,0]
	v_pk_mul_f32 v[22:23], v[94:95], s[14:15] op_sel_hi:[1,0]
	v_pk_mul_f32 v[26:27], v[16:17], v[20:21]
	v_pk_mul_f32 v[20:21], v[14:15], v[22:23]
	v_pk_mul_f32 v[22:23], v[92:93], s[14:15] op_sel_hi:[1,0]
	v_cvt_pk_bf16_f32 v20, v20, v21
	v_cvt_pk_bf16_f32 v21, v26, v27
	v_add_co_u32_e32 v26, vcc, s66, v18
	v_pk_mul_f32 v[30:31], v[22:23], v[12:13]
	v_pk_mul_f32 v[22:23], v[28:29], v[10:11]
	v_addc_co_u32_e32 v27, vcc, 0, v19, vcc
	v_cvt_pk_bf16_f32 v22, v22, v23
	v_cvt_pk_bf16_f32 v23, v30, v31
	global_store_dwordx4 v[26:27], v[20:23], off
	v_pk_mul_f32 v[28:29], v[78:79], s[14:15] op_sel_hi:[1,0]
	s_nop 0
	v_pk_mul_f32 v[20:21], v[88:89], s[14:15] op_sel_hi:[1,0]
	v_pk_mul_f32 v[22:23], v[86:87], s[14:15] op_sel_hi:[1,0]
	v_pk_mul_f32 v[26:27], v[20:21], v[8:9]
	v_pk_mul_f32 v[20:21], v[22:23], v[6:7]
	v_pk_mul_f32 v[22:23], v[80:81], s[14:15] op_sel_hi:[1,0]
	v_cvt_pk_bf16_f32 v20, v20, v21
	v_cvt_pk_bf16_f32 v21, v26, v27
	s_nop 0
	v_pk_mul_f32 v[30:31], v[22:23], v[4:5]
	v_pk_mul_f32 v[22:23], v[28:29], v[2:3]
	v_pk_mul_f32 v[28:29], v[74:75], s[14:15] op_sel_hi:[1,0]
	v_cvt_pk_bf16_f32 v22, v22, v23
	v_cvt_pk_bf16_f32 v23, v30, v31
	global_store_dwordx4 v[24:25], v[20:23], off offset:256
	v_lshl_add_u64 v[24:25], v[18:19], 0, s[18:19]
	s_nop 0
	v_pk_mul_f32 v[20:21], v[84:85], s[14:15] op_sel_hi:[1,0]
	v_pk_mul_f32 v[22:23], v[82:83], s[14:15] op_sel_hi:[1,0]
	v_pk_mul_f32 v[26:27], v[16:17], v[20:21]
	v_pk_mul_f32 v[20:21], v[14:15], v[22:23]
	v_pk_mul_f32 v[22:23], v[76:77], s[14:15] op_sel_hi:[1,0]
	v_cvt_pk_bf16_f32 v20, v20, v21
	v_cvt_pk_bf16_f32 v21, v26, v27
	v_add_co_u32_e32 v26, vcc, s67, v18
	v_pk_mul_f32 v[30:31], v[22:23], v[12:13]
	v_pk_mul_f32 v[22:23], v[28:29], v[10:11]
	v_addc_co_u32_e32 v27, vcc, 0, v19, vcc
	v_cvt_pk_bf16_f32 v22, v22, v23
	v_cvt_pk_bf16_f32 v23, v30, v31
	global_store_dwordx4 v[26:27], v[20:23], off
	v_pk_mul_f32 v[28:29], v[62:63], s[14:15] op_sel_hi:[1,0]
	s_nop 0
	v_pk_mul_f32 v[20:21], v[72:73], s[14:15] op_sel_hi:[1,0]
	v_pk_mul_f32 v[22:23], v[70:71], s[14:15] op_sel_hi:[1,0]
	v_pk_mul_f32 v[26:27], v[20:21], v[8:9]
	v_pk_mul_f32 v[20:21], v[22:23], v[6:7]
	v_pk_mul_f32 v[22:23], v[64:65], s[14:15] op_sel_hi:[1,0]
	v_cvt_pk_bf16_f32 v20, v20, v21
	v_cvt_pk_bf16_f32 v21, v26, v27
	s_nop 0
	v_pk_mul_f32 v[30:31], v[22:23], v[4:5]
	v_pk_mul_f32 v[22:23], v[28:29], v[2:3]
	v_pk_mul_f32 v[28:29], v[58:59], s[14:15] op_sel_hi:[1,0]
	v_cvt_pk_bf16_f32 v22, v22, v23
	v_cvt_pk_bf16_f32 v23, v30, v31
	global_store_dwordx4 v[24:25], v[20:23], off offset:256
	v_lshl_add_u64 v[24:25], v[18:19], 0, s[20:21]
	s_nop 0
	v_pk_mul_f32 v[20:21], v[68:69], s[14:15] op_sel_hi:[1,0]
	v_pk_mul_f32 v[22:23], v[66:67], s[14:15] op_sel_hi:[1,0]
	v_pk_mul_f32 v[26:27], v[16:17], v[20:21]
	v_pk_mul_f32 v[20:21], v[14:15], v[22:23]
	v_pk_mul_f32 v[22:23], v[60:61], s[14:15] op_sel_hi:[1,0]
	v_cvt_pk_bf16_f32 v20, v20, v21
	v_cvt_pk_bf16_f32 v21, v26, v27
	v_add_co_u32_e32 v26, vcc, s68, v18
	v_pk_mul_f32 v[30:31], v[22:23], v[12:13]
	v_pk_mul_f32 v[22:23], v[28:29], v[10:11]
	v_addc_co_u32_e32 v27, vcc, 0, v19, vcc
	v_cvt_pk_bf16_f32 v22, v22, v23
	v_cvt_pk_bf16_f32 v23, v30, v31
	global_store_dwordx4 v[26:27], v[20:23], off
	v_pk_mul_f32 v[28:29], v[46:47], s[14:15] op_sel_hi:[1,0]
	s_nop 0
	v_pk_mul_f32 v[20:21], v[56:57], s[14:15] op_sel_hi:[1,0]
	v_pk_mul_f32 v[22:23], v[54:55], s[14:15] op_sel_hi:[1,0]
	v_pk_mul_f32 v[26:27], v[20:21], v[8:9]
	v_pk_mul_f32 v[20:21], v[22:23], v[6:7]
	v_pk_mul_f32 v[22:23], v[48:49], s[14:15] op_sel_hi:[1,0]
	v_cvt_pk_bf16_f32 v20, v20, v21
	v_cvt_pk_bf16_f32 v21, v26, v27
	s_nop 0
	v_pk_mul_f32 v[30:31], v[22:23], v[4:5]
	v_pk_mul_f32 v[22:23], v[28:29], v[2:3]
	s_nop 0
	v_cvt_pk_bf16_f32 v22, v22, v23
	v_cvt_pk_bf16_f32 v23, v30, v31
	global_store_dwordx4 v[24:25], v[20:23], off offset:256
	v_pk_mul_f32 v[24:25], v[50:51], s[14:15] op_sel_hi:[1,0]
	s_nop 0
	v_pk_mul_f32 v[22:23], v[52:53], s[14:15] op_sel_hi:[1,0]
	v_pk_mul_f32 v[14:15], v[14:15], v[24:25]
	v_pk_mul_f32 v[16:17], v[16:17], v[22:23]
	v_pk_mul_f32 v[22:23], v[44:45], s[14:15] op_sel_hi:[1,0]
	v_pk_mul_f32 v[24:25], v[42:43], s[14:15] op_sel_hi:[1,0]
	v_pk_mul_f32 v[22:23], v[22:23], v[12:13]
	v_pk_mul_f32 v[12:13], v[24:25], v[10:11]
	v_cvt_pk_bf16_f32 v10, v14, v15
	v_add_co_u32_e32 v14, vcc, s69, v18
	v_cvt_pk_bf16_f32 v11, v16, v17
	v_cvt_pk_bf16_f32 v12, v12, v13
	v_cvt_pk_bf16_f32 v13, v22, v23
	v_lshl_add_u64 v[20:21], v[18:19], 0, s[22:23]
	s_nop 0
	v_addc_co_u32_e32 v15, vcc, 0, v19, vcc
	global_store_dwordx4 v[14:15], v[10:13], off
	s_andn2_b64 vcc, exec, s[52:53]
	s_mov_b64 s[52:53], -1
	v_pk_mul_f32 v[10:11], v[40:41], s[14:15] op_sel_hi:[1,0]
	v_pk_mul_f32 v[12:13], v[38:39], s[14:15] op_sel_hi:[1,0]
	v_pk_mul_f32 v[8:9], v[10:11], v[8:9]
	v_pk_mul_f32 v[6:7], v[12:13], v[6:7]
	v_pk_mul_f32 v[10:11], v[36:37], s[14:15] op_sel_hi:[1,0]
	v_pk_mul_f32 v[12:13], v[34:35], s[14:15] op_sel_hi:[1,0]
	v_pk_mul_f32 v[10:11], v[10:11], v[4:5]
	v_pk_mul_f32 v[4:5], v[12:13], v[2:3]
	v_cvt_pk_bf16_f32 v2, v6, v7
	v_cvt_pk_bf16_f32 v3, v8, v9
	s_nop 0
	v_cvt_pk_bf16_f32 v4, v4, v5
	v_cvt_pk_bf16_f32 v5, v10, v11
	global_store_dwordx4 v[20:21], v[2:5], off offset:256
	s_cbranch_vccnz .LBB0_1335
	s_andn2_b64 vcc, exec, s[6:7]
	s_cbranch_vccnz .LBB0_1334
	s_barrier
	s_branch .LBB0_1334

.LBB0_2077:
	v_lshl_or_b32 v20, s53, 7, v219
	v_ashrrev_i32_e32 v21, 31, v20
	s_nop 15
	s_nop 0
	s_nop 0
	s_nop 0
	v_lshl_add_u32 v22, s83, 8, v217
	s_nop 0
	s_mov_b32 s90, 0x3c800000
	s_mov_b32 s92, 0xc01d265f
	s_mov_b32 s94, 0x3fb8aa3b
	s_mov_b32 s96, 1.0
	v_pk_fma_f32 v[28:29], v[190:191], s[90:91], v[238:239] op_sel_hi:[1,0,1]
	v_pk_fma_f32 v[30:31], v[192:193], s[90:91], v[240:241] op_sel_hi:[1,0,1]
	v_min_f32_e32 v28, 0x40e00000, v28
	v_min_f32_e32 v29, 0x40e00000, v29
	v_min_f32_e32 v30, 0x40e00000, v30
	v_min_f32_e32 v31, 0x40e00000, v31
	v_pk_mul_f32 v[32:33], v[28:29], s[92:93] op_sel_hi:[1,0]
	v_pk_mul_f32 v[34:35], v[30:31], s[92:93] op_sel_hi:[1,0]
	v_exp_f32_e32 v32, v32
	v_exp_f32_e32 v33, v33
	v_exp_f32_e32 v34, v34
	v_exp_f32_e32 v35, v35
	v_pk_add_f32 v[32:33], v[32:33], s[96:97] op_sel_hi:[1,0]
	v_pk_add_f32 v[34:35], v[34:35], s[96:97] op_sel_hi:[1,0]
	v_rcp_f32_e32 v32, v32
	v_rcp_f32_e32 v33, v33
	v_rcp_f32_e32 v34, v34
	v_rcp_f32_e32 v35, v35
	v_pk_mul_f32 v[28:29], v[28:29], v[32:33]
	v_pk_mul_f32 v[30:31], v[30:31], v[34:35]
	v_pk_fma_f32 v[32:33], v[186:187], s[90:91], v[246:247] op_sel_hi:[1,0,1]
	v_pk_fma_f32 v[34:35], v[188:189], s[90:91], v[248:249] op_sel_hi:[1,0,1]
	v_med3_f32 v32, v32, s79, v224
	v_med3_f32 v33, v33, s79, v224
	v_med3_f32 v34, v34, s79, v224
	v_med3_f32 v35, v35, s79, v224
	v_fma_f32 v32, v32, 4.0, 4.0
	v_fma_f32 v33, v33, 4.0, 4.0
	v_fma_f32 v34, v34, 4.0, 4.0
	v_fma_f32 v35, v35, 4.0, 4.0
	v_pk_mul_f32 v[28:29], v[32:33], v[28:29]
	v_pk_mul_f32 v[30:31], v[34:35], v[30:31]
	v_pk_fma_f32 v[36:37], v[182:183], s[90:91], v[242:243] op_sel_hi:[1,0,1]
	v_pk_fma_f32 v[38:39], v[184:185], s[90:91], v[244:245] op_sel_hi:[1,0,1]
	v_min_f32_e32 v36, 0x40e00000, v36
	v_min_f32_e32 v37, 0x40e00000, v37
	v_min_f32_e32 v38, 0x40e00000, v38
	v_min_f32_e32 v39, 0x40e00000, v39
	v_pk_mul_f32 v[32:33], v[36:37], s[92:93] op_sel_hi:[1,0]
	v_pk_mul_f32 v[34:35], v[38:39], s[92:93] op_sel_hi:[1,0]
	v_exp_f32_e32 v32, v32
	v_exp_f32_e32 v33, v33
	v_exp_f32_e32 v34, v34
	v_exp_f32_e32 v35, v35
	v_pk_add_f32 v[32:33], v[32:33], s[96:97] op_sel_hi:[1,0]
	v_pk_add_f32 v[34:35], v[34:35], s[96:97] op_sel_hi:[1,0]
	v_rcp_f32_e32 v32, v32
	v_rcp_f32_e32 v33, v33
	v_rcp_f32_e32 v34, v34
	v_rcp_f32_e32 v35, v35
	v_pk_mul_f32 v[36:37], v[36:37], v[32:33]
	v_pk_mul_f32 v[38:39], v[38:39], v[34:35]
	v_pk_fma_f32 v[32:33], v[178:179], s[90:91], v[250:251] op_sel_hi:[1,0,1]
	v_pk_fma_f32 v[34:35], v[180:181], s[90:91], v[252:253] op_sel_hi:[1,0,1]
	v_med3_f32 v32, v32, s79, v224
	v_med3_f32 v33, v33, s79, v224
	v_med3_f32 v34, v34, s79, v224
	v_med3_f32 v35, v35, s79, v224
	v_fma_f32 v32, v32, 4.0, 4.0
	v_fma_f32 v33, v33, 4.0, 4.0
	v_fma_f32 v34, v34, 4.0, 4.0
	v_fma_f32 v35, v35, 4.0, 4.0
	v_pk_mul_f32 v[36:37], v[32:33], v[36:37]
	v_pk_mul_f32 v[38:39], v[34:35], v[38:39]
	v_ashrrev_i32_e32 v23, 31, v22
	v_lshlrev_b64 v[18:19], 11, v[22:23]
	v_lshl_add_u64 v[18:19], s[6:7], 0, v[18:19]
	v_lshl_add_u64 v[18:19], v[18:19], 0, v[20:21]
	v_mov_b32_e32 v24, v201
	v_mov_b32_e32 v25, v201
	v_cvt_pk_fp8_f32 v24, v28, v29
	v_cvt_pk_fp8_f32 v25, v36, v37
	v_cvt_pk_fp8_f32 v24, v30, v31 op_sel:[0,0,1]
	v_cvt_pk_fp8_f32 v25, v38, v39 op_sel:[0,0,1]
	global_store_dwordx2 v[18:19], v[24:25], off
	v_pk_fma_f32 v[28:29], v[174:175], s[90:91], v[238:239] op_sel_hi:[1,0,1]
	v_pk_fma_f32 v[30:31], v[176:177], s[90:91], v[240:241] op_sel_hi:[1,0,1]
	v_min_f32_e32 v28, 0x40e00000, v28
	v_min_f32_e32 v29, 0x40e00000, v29
	v_min_f32_e32 v30, 0x40e00000, v30
	v_min_f32_e32 v31, 0x40e00000, v31
	v_pk_mul_f32 v[32:33], v[28:29], s[92:93] op_sel_hi:[1,0]
	v_pk_mul_f32 v[34:35], v[30:31], s[92:93] op_sel_hi:[1,0]
	v_exp_f32_e32 v32, v32
	v_exp_f32_e32 v33, v33
	v_exp_f32_e32 v34, v34
	v_exp_f32_e32 v35, v35
	v_pk_add_f32 v[32:33], v[32:33], s[96:97] op_sel_hi:[1,0]
	v_pk_add_f32 v[34:35], v[34:35], s[96:97] op_sel_hi:[1,0]
	v_rcp_f32_e32 v32, v32
	v_rcp_f32_e32 v33, v33
	v_rcp_f32_e32 v34, v34
	v_rcp_f32_e32 v35, v35
	v_pk_mul_f32 v[28:29], v[28:29], v[32:33]
	v_pk_mul_f32 v[30:31], v[30:31], v[34:35]
	v_pk_fma_f32 v[32:33], v[170:171], s[90:91], v[246:247] op_sel_hi:[1,0,1]
	v_pk_fma_f32 v[34:35], v[172:173], s[90:91], v[248:249] op_sel_hi:[1,0,1]
	v_med3_f32 v32, v32, s79, v224
	v_med3_f32 v33, v33, s79, v224
	v_med3_f32 v34, v34, s79, v224
	v_med3_f32 v35, v35, s79, v224
	v_fma_f32 v32, v32, 4.0, 4.0
	v_fma_f32 v33, v33, 4.0, 4.0
	v_fma_f32 v34, v34, 4.0, 4.0
	v_fma_f32 v35, v35, 4.0, 4.0
	v_pk_mul_f32 v[28:29], v[32:33], v[28:29]
	v_pk_mul_f32 v[30:31], v[34:35], v[30:31]
	v_pk_fma_f32 v[36:37], v[166:167], s[90:91], v[242:243] op_sel_hi:[1,0,1]
	v_pk_fma_f32 v[38:39], v[168:169], s[90:91], v[244:245] op_sel_hi:[1,0,1]
	v_min_f32_e32 v36, 0x40e00000, v36
	v_min_f32_e32 v37, 0x40e00000, v37
	v_min_f32_e32 v38, 0x40e00000, v38
	v_min_f32_e32 v39, 0x40e00000, v39
	v_pk_mul_f32 v[32:33], v[36:37], s[92:93] op_sel_hi:[1,0]
	v_pk_mul_f32 v[34:35], v[38:39], s[92:93] op_sel_hi:[1,0]
	v_exp_f32_e32 v32, v32
	v_exp_f32_e32 v33, v33
	v_exp_f32_e32 v34, v34
	v_exp_f32_e32 v35, v35
	v_pk_add_f32 v[32:33], v[32:33], s[96:97] op_sel_hi:[1,0]
	v_pk_add_f32 v[34:35], v[34:35], s[96:97] op_sel_hi:[1,0]
	v_rcp_f32_e32 v32, v32
	v_rcp_f32_e32 v33, v33
	v_rcp_f32_e32 v34, v34
	v_rcp_f32_e32 v35, v35
	v_pk_mul_f32 v[36:37], v[36:37], v[32:33]
	v_pk_mul_f32 v[38:39], v[38:39], v[34:35]
	v_pk_fma_f32 v[32:33], v[162:163], s[90:91], v[250:251] op_sel_hi:[1,0,1]
	v_pk_fma_f32 v[34:35], v[164:165], s[90:91], v[252:253] op_sel_hi:[1,0,1]
	v_med3_f32 v32, v32, s79, v224
	v_med3_f32 v33, v33, s79, v224
	v_med3_f32 v34, v34, s79, v224
	v_med3_f32 v35, v35, s79, v224
	v_fma_f32 v32, v32, 4.0, 4.0
	v_fma_f32 v33, v33, 4.0, 4.0
	v_fma_f32 v34, v34, 4.0, 4.0
	v_fma_f32 v35, v35, 4.0, 4.0
	v_pk_mul_f32 v[36:37], v[32:33], v[36:37]
	v_pk_mul_f32 v[38:39], v[34:35], v[38:39]
	v_or_b32_e32 v26, 16, v22
	v_ashrrev_i32_e32 v27, 31, v26
	v_lshlrev_b64 v[26:27], 11, v[26:27]
	v_lshl_add_u64 v[26:27], s[6:7], 0, v[26:27]
	v_lshl_add_u64 v[26:27], v[26:27], 0, v[20:21]
	v_mov_b32_e32 v24, v201
	v_mov_b32_e32 v25, v201
	v_cvt_pk_fp8_f32 v24, v28, v29
	v_cvt_pk_fp8_f32 v25, v36, v37
	v_cvt_pk_fp8_f32 v24, v30, v31 op_sel:[0,0,1]
	v_cvt_pk_fp8_f32 v25, v38, v39 op_sel:[0,0,1]
	global_store_dwordx2 v[26:27], v[24:25], off
	v_pk_fma_f32 v[28:29], v[158:159], s[90:91], v[238:239] op_sel_hi:[1,0,1]
	v_pk_fma_f32 v[30:31], v[160:161], s[90:91], v[240:241] op_sel_hi:[1,0,1]
	v_min_f32_e32 v28, 0x40e00000, v28
	v_min_f32_e32 v29, 0x40e00000, v29
	v_min_f32_e32 v30, 0x40e00000, v30
	v_min_f32_e32 v31, 0x40e00000, v31
	v_pk_mul_f32 v[32:33], v[28:29], s[92:93] op_sel_hi:[1,0]
	v_pk_mul_f32 v[34:35], v[30:31], s[92:93] op_sel_hi:[1,0]
	v_exp_f32_e32 v32, v32
	v_exp_f32_e32 v33, v33
	v_exp_f32_e32 v34, v34
	v_exp_f32_e32 v35, v35
	v_pk_add_f32 v[32:33], v[32:33], s[96:97] op_sel_hi:[1,0]
	v_pk_add_f32 v[34:35], v[34:35], s[96:97] op_sel_hi:[1,0]
	v_rcp_f32_e32 v32, v32
	v_rcp_f32_e32 v33, v33
	v_rcp_f32_e32 v34, v34
	v_rcp_f32_e32 v35, v35
	v_pk_mul_f32 v[28:29], v[28:29], v[32:33]
	v_pk_mul_f32 v[30:31], v[30:31], v[34:35]
	v_pk_fma_f32 v[32:33], v[154:155], s[90:91], v[246:247] op_sel_hi:[1,0,1]
	v_pk_fma_f32 v[34:35], v[156:157], s[90:91], v[248:249] op_sel_hi:[1,0,1]
	v_med3_f32 v32, v32, s79, v224
	v_med3_f32 v33, v33, s79, v224
	v_med3_f32 v34, v34, s79, v224
	v_med3_f32 v35, v35, s79, v224
	v_fma_f32 v32, v32, 4.0, 4.0
	v_fma_f32 v33, v33, 4.0, 4.0
	v_fma_f32 v34, v34, 4.0, 4.0
	v_fma_f32 v35, v35, 4.0, 4.0
	v_pk_mul_f32 v[28:29], v[32:33], v[28:29]
	v_pk_mul_f32 v[30:31], v[34:35], v[30:31]
	v_pk_fma_f32 v[36:37], v[150:151], s[90:91], v[242:243] op_sel_hi:[1,0,1]
	v_pk_fma_f32 v[38:39], v[152:153], s[90:91], v[244:245] op_sel_hi:[1,0,1]
	v_min_f32_e32 v36, 0x40e00000, v36
	v_min_f32_e32 v37, 0x40e00000, v37
	v_min_f32_e32 v38, 0x40e00000, v38
	v_min_f32_e32 v39, 0x40e00000, v39
	v_pk_mul_f32 v[32:33], v[36:37], s[92:93] op_sel_hi:[1,0]
	v_pk_mul_f32 v[34:35], v[38:39], s[92:93] op_sel_hi:[1,0]
	v_exp_f32_e32 v32, v32
	v_exp_f32_e32 v33, v33
	v_exp_f32_e32 v34, v34
	v_exp_f32_e32 v35, v35
	v_pk_add_f32 v[32:33], v[32:33], s[96:97] op_sel_hi:[1,0]
	v_pk_add_f32 v[34:35], v[34:35], s[96:97] op_sel_hi:[1,0]
	v_rcp_f32_e32 v32, v32
	v_rcp_f32_e32 v33, v33
	v_rcp_f32_e32 v34, v34
	v_rcp_f32_e32 v35, v35
	v_pk_mul_f32 v[36:37], v[36:37], v[32:33]
	v_pk_mul_f32 v[38:39], v[38:39], v[34:35]
	v_pk_fma_f32 v[32:33], v[146:147], s[90:91], v[250:251] op_sel_hi:[1,0,1]
	v_pk_fma_f32 v[34:35], v[148:149], s[90:91], v[252:253] op_sel_hi:[1,0,1]
	v_med3_f32 v32, v32, s79, v224
	v_med3_f32 v33, v33, s79, v224
	v_med3_f32 v34, v34, s79, v224
	v_med3_f32 v35, v35, s79, v224
	v_fma_f32 v32, v32, 4.0, 4.0
	v_fma_f32 v33, v33, 4.0, 4.0
	v_fma_f32 v34, v34, 4.0, 4.0
	v_fma_f32 v35, v35, 4.0, 4.0
	v_pk_mul_f32 v[36:37], v[32:33], v[36:37]
	v_pk_mul_f32 v[38:39], v[34:35], v[38:39]
	v_or_b32_e32 v26, 32, v22
	v_ashrrev_i32_e32 v27, 31, v26
	v_lshlrev_b64 v[26:27], 11, v[26:27]
	v_lshl_add_u64 v[26:27], s[6:7], 0, v[26:27]
	v_lshl_add_u64 v[26:27], v[26:27], 0, v[20:21]
	v_mov_b32_e32 v24, v201
	v_mov_b32_e32 v25, v201
	v_cvt_pk_fp8_f32 v24, v28, v29
	v_cvt_pk_fp8_f32 v25, v36, v37
	v_cvt_pk_fp8_f32 v24, v30, v31 op_sel:[0,0,1]
	v_cvt_pk_fp8_f32 v25, v38, v39 op_sel:[0,0,1]
	global_store_dwordx2 v[26:27], v[24:25], off
	v_pk_fma_f32 v[28:29], v[142:143], s[90:91], v[238:239] op_sel_hi:[1,0,1]
	v_pk_fma_f32 v[30:31], v[144:145], s[90:91], v[240:241] op_sel_hi:[1,0,1]
	v_min_f32_e32 v28, 0x40e00000, v28
	v_min_f32_e32 v29, 0x40e00000, v29
	v_min_f32_e32 v30, 0x40e00000, v30
	v_min_f32_e32 v31, 0x40e00000, v31
	v_pk_mul_f32 v[32:33], v[28:29], s[92:93] op_sel_hi:[1,0]
	v_pk_mul_f32 v[34:35], v[30:31], s[92:93] op_sel_hi:[1,0]
	v_exp_f32_e32 v32, v32
	v_exp_f32_e32 v33, v33
	v_exp_f32_e32 v34, v34
	v_exp_f32_e32 v35, v35
	v_pk_add_f32 v[32:33], v[32:33], s[96:97] op_sel_hi:[1,0]
	v_pk_add_f32 v[34:35], v[34:35], s[96:97] op_sel_hi:[1,0]
	v_rcp_f32_e32 v32, v32
	v_rcp_f32_e32 v33, v33
	v_rcp_f32_e32 v34, v34
	v_rcp_f32_e32 v35, v35
	v_pk_mul_f32 v[28:29], v[28:29], v[32:33]
	v_pk_mul_f32 v[30:31], v[30:31], v[34:35]
	v_pk_fma_f32 v[32:33], v[138:139], s[90:91], v[246:247] op_sel_hi:[1,0,1]
	v_pk_fma_f32 v[34:35], v[140:141], s[90:91], v[248:249] op_sel_hi:[1,0,1]
	v_med3_f32 v32, v32, s79, v224
	v_med3_f32 v33, v33, s79, v224
	v_med3_f32 v34, v34, s79, v224
	v_med3_f32 v35, v35, s79, v224
	v_fma_f32 v32, v32, 4.0, 4.0
	v_fma_f32 v33, v33, 4.0, 4.0
	v_fma_f32 v34, v34, 4.0, 4.0
	v_fma_f32 v35, v35, 4.0, 4.0
	v_pk_mul_f32 v[28:29], v[32:33], v[28:29]
	v_pk_mul_f32 v[30:31], v[34:35], v[30:31]
	v_pk_fma_f32 v[36:37], v[134:135], s[90:91], v[242:243] op_sel_hi:[1,0,1]
	v_pk_fma_f32 v[38:39], v[136:137], s[90:91], v[244:245] op_sel_hi:[1,0,1]
	v_min_f32_e32 v36, 0x40e00000, v36
	v_min_f32_e32 v37, 0x40e00000, v37
	v_min_f32_e32 v38, 0x40e00000, v38
	v_min_f32_e32 v39, 0x40e00000, v39
	v_pk_mul_f32 v[32:33], v[36:37], s[92:93] op_sel_hi:[1,0]
	v_pk_mul_f32 v[34:35], v[38:39], s[92:93] op_sel_hi:[1,0]
	v_exp_f32_e32 v32, v32
	v_exp_f32_e32 v33, v33
	v_exp_f32_e32 v34, v34
	v_exp_f32_e32 v35, v35
	v_pk_add_f32 v[32:33], v[32:33], s[96:97] op_sel_hi:[1,0]
	v_pk_add_f32 v[34:35], v[34:35], s[96:97] op_sel_hi:[1,0]
	v_rcp_f32_e32 v32, v32
	v_rcp_f32_e32 v33, v33
	v_rcp_f32_e32 v34, v34
	v_rcp_f32_e32 v35, v35
	v_pk_mul_f32 v[36:37], v[36:37], v[32:33]
	v_pk_mul_f32 v[38:39], v[38:39], v[34:35]
	v_pk_fma_f32 v[32:33], v[130:131], s[90:91], v[250:251] op_sel_hi:[1,0,1]
	v_pk_fma_f32 v[34:35], v[132:133], s[90:91], v[252:253] op_sel_hi:[1,0,1]
	v_med3_f32 v32, v32, s79, v224
	v_med3_f32 v33, v33, s79, v224
	v_med3_f32 v34, v34, s79, v224
	v_med3_f32 v35, v35, s79, v224
	v_fma_f32 v32, v32, 4.0, 4.0
	v_fma_f32 v33, v33, 4.0, 4.0
	v_fma_f32 v34, v34, 4.0, 4.0
	v_fma_f32 v35, v35, 4.0, 4.0
	v_pk_mul_f32 v[36:37], v[32:33], v[36:37]
	v_pk_mul_f32 v[38:39], v[34:35], v[38:39]
	v_or_b32_e32 v22, 48, v22
	v_ashrrev_i32_e32 v23, 31, v22
	v_lshlrev_b64 v[22:23], 11, v[22:23]
	v_lshl_add_u64 v[22:23], s[6:7], 0, v[22:23]
	v_lshl_add_u64 v[20:21], v[22:23], 0, v[20:21]
	v_mov_b32_e32 v24, v201
	v_mov_b32_e32 v25, v201
	v_cvt_pk_fp8_f32 v24, v28, v29
	v_cvt_pk_fp8_f32 v25, v36, v37
	v_cvt_pk_fp8_f32 v24, v30, v31 op_sel:[0,0,1]
	v_cvt_pk_fp8_f32 v25, v38, v39 op_sel:[0,0,1]
	global_store_dwordx2 v[20:21], v[24:25], off
	v_pk_fma_f32 v[28:29], v[126:127], s[90:91], v[238:239] op_sel_hi:[1,0,1]
	v_pk_fma_f32 v[30:31], v[128:129], s[90:91], v[240:241] op_sel_hi:[1,0,1]
	v_min_f32_e32 v28, 0x40e00000, v28
	v_min_f32_e32 v29, 0x40e00000, v29
	v_min_f32_e32 v30, 0x40e00000, v30
	v_min_f32_e32 v31, 0x40e00000, v31
	v_pk_mul_f32 v[32:33], v[28:29], s[92:93] op_sel_hi:[1,0]
	v_pk_mul_f32 v[34:35], v[30:31], s[92:93] op_sel_hi:[1,0]
	v_exp_f32_e32 v32, v32
	v_exp_f32_e32 v33, v33
	v_exp_f32_e32 v34, v34
	v_exp_f32_e32 v35, v35
	v_pk_add_f32 v[32:33], v[32:33], s[96:97] op_sel_hi:[1,0]
	v_pk_add_f32 v[34:35], v[34:35], s[96:97] op_sel_hi:[1,0]
	v_rcp_f32_e32 v32, v32
	v_rcp_f32_e32 v33, v33
	v_rcp_f32_e32 v34, v34
	v_rcp_f32_e32 v35, v35
	v_pk_mul_f32 v[28:29], v[28:29], v[32:33]
	v_pk_mul_f32 v[30:31], v[30:31], v[34:35]
	v_pk_fma_f32 v[32:33], v[122:123], s[90:91], v[246:247] op_sel_hi:[1,0,1]
	v_pk_fma_f32 v[34:35], v[124:125], s[90:91], v[248:249] op_sel_hi:[1,0,1]
	v_med3_f32 v32, v32, s79, v224
	v_med3_f32 v33, v33, s79, v224
	v_med3_f32 v34, v34, s79, v224
	v_med3_f32 v35, v35, s79, v224
	v_fma_f32 v32, v32, 4.0, 4.0
	v_fma_f32 v33, v33, 4.0, 4.0
	v_fma_f32 v34, v34, 4.0, 4.0
	v_fma_f32 v35, v35, 4.0, 4.0
	v_pk_mul_f32 v[28:29], v[32:33], v[28:29]
	v_pk_mul_f32 v[30:31], v[34:35], v[30:31]
	v_pk_fma_f32 v[36:37], v[118:119], s[90:91], v[242:243] op_sel_hi:[1,0,1]
	v_pk_fma_f32 v[38:39], v[120:121], s[90:91], v[244:245] op_sel_hi:[1,0,1]
	v_min_f32_e32 v36, 0x40e00000, v36
	v_min_f32_e32 v37, 0x40e00000, v37
	v_min_f32_e32 v38, 0x40e00000, v38
	v_min_f32_e32 v39, 0x40e00000, v39
	v_pk_mul_f32 v[32:33], v[36:37], s[92:93] op_sel_hi:[1,0]
	v_pk_mul_f32 v[34:35], v[38:39], s[92:93] op_sel_hi:[1,0]
	v_exp_f32_e32 v32, v32
	v_exp_f32_e32 v33, v33
	v_exp_f32_e32 v34, v34
	v_exp_f32_e32 v35, v35
	v_pk_add_f32 v[32:33], v[32:33], s[96:97] op_sel_hi:[1,0]
	v_pk_add_f32 v[34:35], v[34:35], s[96:97] op_sel_hi:[1,0]
	v_rcp_f32_e32 v32, v32
	v_rcp_f32_e32 v33, v33
	v_rcp_f32_e32 v34, v34
	v_rcp_f32_e32 v35, v35
	v_pk_mul_f32 v[36:37], v[36:37], v[32:33]
	v_pk_mul_f32 v[38:39], v[38:39], v[34:35]
	v_pk_fma_f32 v[32:33], v[114:115], s[90:91], v[250:251] op_sel_hi:[1,0,1]
	v_pk_fma_f32 v[34:35], v[116:117], s[90:91], v[252:253] op_sel_hi:[1,0,1]
	v_med3_f32 v32, v32, s79, v224
	v_med3_f32 v33, v33, s79, v224
	v_med3_f32 v34, v34, s79, v224
	v_med3_f32 v35, v35, s79, v224
	v_fma_f32 v32, v32, 4.0, 4.0
	v_fma_f32 v33, v33, 4.0, 4.0
	v_fma_f32 v34, v34, 4.0, 4.0
	v_fma_f32 v35, v35, 4.0, 4.0
	v_pk_mul_f32 v[36:37], v[32:33], v[36:37]
	v_pk_mul_f32 v[38:39], v[34:35], v[38:39]
	v_add_co_u32_e32 v22, vcc, s80, v18
	s_nop 0
	v_addc_co_u32_e32 v23, vcc, 0, v19, vcc
	v_mov_b32_e32 v20, v201
	v_mov_b32_e32 v21, v201
	v_cvt_pk_fp8_f32 v20, v28, v29
	v_cvt_pk_fp8_f32 v21, v36, v37
	v_cvt_pk_fp8_f32 v20, v30, v31 op_sel:[0,0,1]
	v_cvt_pk_fp8_f32 v21, v38, v39 op_sel:[0,0,1]
	global_store_dwordx2 v[22:23], v[20:21], off
	v_pk_fma_f32 v[28:29], v[110:111], s[90:91], v[238:239] op_sel_hi:[1,0,1]
	v_pk_fma_f32 v[30:31], v[112:113], s[90:91], v[240:241] op_sel_hi:[1,0,1]
	v_min_f32_e32 v28, 0x40e00000, v28
	v_min_f32_e32 v29, 0x40e00000, v29
	v_min_f32_e32 v30, 0x40e00000, v30
	v_min_f32_e32 v31, 0x40e00000, v31
	v_pk_mul_f32 v[32:33], v[28:29], s[92:93] op_sel_hi:[1,0]
	v_pk_mul_f32 v[34:35], v[30:31], s[92:93] op_sel_hi:[1,0]
	v_exp_f32_e32 v32, v32
	v_exp_f32_e32 v33, v33
	v_exp_f32_e32 v34, v34
	v_exp_f32_e32 v35, v35
	v_pk_add_f32 v[32:33], v[32:33], s[96:97] op_sel_hi:[1,0]
	v_pk_add_f32 v[34:35], v[34:35], s[96:97] op_sel_hi:[1,0]
	v_rcp_f32_e32 v32, v32
	v_rcp_f32_e32 v33, v33
	v_rcp_f32_e32 v34, v34
	v_rcp_f32_e32 v35, v35
	v_pk_mul_f32 v[28:29], v[28:29], v[32:33]
	v_pk_mul_f32 v[30:31], v[30:31], v[34:35]
	v_pk_fma_f32 v[32:33], v[106:107], s[90:91], v[246:247] op_sel_hi:[1,0,1]
	v_pk_fma_f32 v[34:35], v[108:109], s[90:91], v[248:249] op_sel_hi:[1,0,1]
	v_med3_f32 v32, v32, s79, v224
	v_med3_f32 v33, v33, s79, v224
	v_med3_f32 v34, v34, s79, v224
	v_med3_f32 v35, v35, s79, v224
	v_fma_f32 v32, v32, 4.0, 4.0
	v_fma_f32 v33, v33, 4.0, 4.0
	v_fma_f32 v34, v34, 4.0, 4.0
	v_fma_f32 v35, v35, 4.0, 4.0
	v_pk_mul_f32 v[28:29], v[32:33], v[28:29]
	v_pk_mul_f32 v[30:31], v[34:35], v[30:31]
	v_pk_fma_f32 v[36:37], v[102:103], s[90:91], v[242:243] op_sel_hi:[1,0,1]
	v_pk_fma_f32 v[38:39], v[104:105], s[90:91], v[244:245] op_sel_hi:[1,0,1]
	v_min_f32_e32 v36, 0x40e00000, v36
	v_min_f32_e32 v37, 0x40e00000, v37
	v_min_f32_e32 v38, 0x40e00000, v38
	v_min_f32_e32 v39, 0x40e00000, v39
	v_pk_mul_f32 v[32:33], v[36:37], s[92:93] op_sel_hi:[1,0]
	v_pk_mul_f32 v[34:35], v[38:39], s[92:93] op_sel_hi:[1,0]
	v_exp_f32_e32 v32, v32
	v_exp_f32_e32 v33, v33
	v_exp_f32_e32 v34, v34
	v_exp_f32_e32 v35, v35
	v_pk_add_f32 v[32:33], v[32:33], s[96:97] op_sel_hi:[1,0]
	v_pk_add_f32 v[34:35], v[34:35], s[96:97] op_sel_hi:[1,0]
	v_rcp_f32_e32 v32, v32
	v_rcp_f32_e32 v33, v33
	v_rcp_f32_e32 v34, v34
	v_rcp_f32_e32 v35, v35
	v_pk_mul_f32 v[36:37], v[36:37], v[32:33]
	v_pk_mul_f32 v[38:39], v[38:39], v[34:35]
	v_pk_fma_f32 v[32:33], v[98:99], s[90:91], v[250:251] op_sel_hi:[1,0,1]
	v_pk_fma_f32 v[34:35], v[100:101], s[90:91], v[252:253] op_sel_hi:[1,0,1]
	v_med3_f32 v32, v32, s79, v224
	v_med3_f32 v33, v33, s79, v224
	v_med3_f32 v34, v34, s79, v224
	v_med3_f32 v35, v35, s79, v224
	v_fma_f32 v32, v32, 4.0, 4.0
	v_fma_f32 v33, v33, 4.0, 4.0
	v_fma_f32 v34, v34, 4.0, 4.0
	v_fma_f32 v35, v35, 4.0, 4.0
	v_pk_mul_f32 v[36:37], v[32:33], v[36:37]
	v_pk_mul_f32 v[38:39], v[34:35], v[38:39]
	v_add_co_u32_e32 v22, vcc, s81, v18
	s_nop 0
	v_addc_co_u32_e32 v23, vcc, 0, v19, vcc
	v_mov_b32_e32 v20, v201
	v_mov_b32_e32 v21, v201
	v_cvt_pk_fp8_f32 v20, v28, v29
	v_cvt_pk_fp8_f32 v21, v36, v37
	v_cvt_pk_fp8_f32 v20, v30, v31 op_sel:[0,0,1]
	v_cvt_pk_fp8_f32 v21, v38, v39 op_sel:[0,0,1]
	global_store_dwordx2 v[22:23], v[20:21], off
	v_pk_fma_f32 v[28:29], v[94:95], s[90:91], v[238:239] op_sel_hi:[1,0,1]
	v_pk_fma_f32 v[30:31], v[96:97], s[90:91], v[240:241] op_sel_hi:[1,0,1]
	v_min_f32_e32 v28, 0x40e00000, v28
	v_min_f32_e32 v29, 0x40e00000, v29
	v_min_f32_e32 v30, 0x40e00000, v30
	v_min_f32_e32 v31, 0x40e00000, v31
	v_pk_mul_f32 v[32:33], v[28:29], s[92:93] op_sel_hi:[1,0]
	v_pk_mul_f32 v[34:35], v[30:31], s[92:93] op_sel_hi:[1,0]
	v_exp_f32_e32 v32, v32
	v_exp_f32_e32 v33, v33
	v_exp_f32_e32 v34, v34
	v_exp_f32_e32 v35, v35
	v_pk_add_f32 v[32:33], v[32:33], s[96:97] op_sel_hi:[1,0]
	v_pk_add_f32 v[34:35], v[34:35], s[96:97] op_sel_hi:[1,0]
	v_rcp_f32_e32 v32, v32
	v_rcp_f32_e32 v33, v33
	v_rcp_f32_e32 v34, v34
	v_rcp_f32_e32 v35, v35
	v_pk_mul_f32 v[28:29], v[28:29], v[32:33]
	v_pk_mul_f32 v[30:31], v[30:31], v[34:35]
	v_pk_fma_f32 v[32:33], v[90:91], s[90:91], v[246:247] op_sel_hi:[1,0,1]
	v_pk_fma_f32 v[34:35], v[92:93], s[90:91], v[248:249] op_sel_hi:[1,0,1]
	v_med3_f32 v32, v32, s79, v224
	v_med3_f32 v33, v33, s79, v224
	v_med3_f32 v34, v34, s79, v224
	v_med3_f32 v35, v35, s79, v224
	v_fma_f32 v32, v32, 4.0, 4.0
	v_fma_f32 v33, v33, 4.0, 4.0
	v_fma_f32 v34, v34, 4.0, 4.0
	v_fma_f32 v35, v35, 4.0, 4.0
	v_pk_mul_f32 v[28:29], v[32:33], v[28:29]
	v_pk_mul_f32 v[30:31], v[34:35], v[30:31]
	v_pk_fma_f32 v[36:37], v[86:87], s[90:91], v[242:243] op_sel_hi:[1,0,1]
	v_pk_fma_f32 v[38:39], v[88:89], s[90:91], v[244:245] op_sel_hi:[1,0,1]
	v_min_f32_e32 v36, 0x40e00000, v36
	v_min_f32_e32 v37, 0x40e00000, v37
	v_min_f32_e32 v38, 0x40e00000, v38
	v_min_f32_e32 v39, 0x40e00000, v39
	v_pk_mul_f32 v[32:33], v[36:37], s[92:93] op_sel_hi:[1,0]
	v_pk_mul_f32 v[34:35], v[38:39], s[92:93] op_sel_hi:[1,0]
	v_exp_f32_e32 v32, v32
	v_exp_f32_e32 v33, v33
	v_exp_f32_e32 v34, v34
	v_exp_f32_e32 v35, v35
	v_pk_add_f32 v[32:33], v[32:33], s[96:97] op_sel_hi:[1,0]
	v_pk_add_f32 v[34:35], v[34:35], s[96:97] op_sel_hi:[1,0]
	v_rcp_f32_e32 v32, v32
	v_rcp_f32_e32 v33, v33
	v_rcp_f32_e32 v34, v34
	v_rcp_f32_e32 v35, v35
	v_pk_mul_f32 v[36:37], v[36:37], v[32:33]
	v_pk_mul_f32 v[38:39], v[38:39], v[34:35]
	v_pk_fma_f32 v[32:33], v[82:83], s[90:91], v[250:251] op_sel_hi:[1,0,1]
	v_pk_fma_f32 v[34:35], v[84:85], s[90:91], v[252:253] op_sel_hi:[1,0,1]
	v_med3_f32 v32, v32, s79, v224
	v_med3_f32 v33, v33, s79, v224
	v_med3_f32 v34, v34, s79, v224
	v_med3_f32 v35, v35, s79, v224
	v_fma_f32 v32, v32, 4.0, 4.0
	v_fma_f32 v33, v33, 4.0, 4.0
	v_fma_f32 v34, v34, 4.0, 4.0
	v_fma_f32 v35, v35, 4.0, 4.0
	v_pk_mul_f32 v[36:37], v[32:33], v[36:37]
	v_pk_mul_f32 v[38:39], v[34:35], v[38:39]
	v_add_co_u32_e32 v22, vcc, s82, v18
	s_nop 0
	v_addc_co_u32_e32 v23, vcc, 0, v19, vcc
	v_mov_b32_e32 v20, v201
	v_mov_b32_e32 v21, v201
	v_cvt_pk_fp8_f32 v20, v28, v29
	v_cvt_pk_fp8_f32 v21, v36, v37
	v_cvt_pk_fp8_f32 v20, v30, v31 op_sel:[0,0,1]
	v_cvt_pk_fp8_f32 v21, v38, v39 op_sel:[0,0,1]
	global_store_dwordx2 v[22:23], v[20:21], off
	v_pk_fma_f32 v[28:29], v[78:79], s[90:91], v[238:239] op_sel_hi:[1,0,1]
	v_pk_fma_f32 v[30:31], v[80:81], s[90:91], v[240:241] op_sel_hi:[1,0,1]
	v_min_f32_e32 v28, 0x40e00000, v28
	v_min_f32_e32 v29, 0x40e00000, v29
	v_min_f32_e32 v30, 0x40e00000, v30
	v_min_f32_e32 v31, 0x40e00000, v31
	v_pk_mul_f32 v[32:33], v[28:29], s[92:93] op_sel_hi:[1,0]
	v_pk_mul_f32 v[34:35], v[30:31], s[92:93] op_sel_hi:[1,0]
	v_exp_f32_e32 v32, v32
	v_exp_f32_e32 v33, v33
	v_exp_f32_e32 v34, v34
	v_exp_f32_e32 v35, v35
	v_pk_add_f32 v[32:33], v[32:33], s[96:97] op_sel_hi:[1,0]
	v_pk_add_f32 v[34:35], v[34:35], s[96:97] op_sel_hi:[1,0]
	v_rcp_f32_e32 v32, v32
	v_rcp_f32_e32 v33, v33
	v_rcp_f32_e32 v34, v34
	v_rcp_f32_e32 v35, v35
	v_pk_mul_f32 v[28:29], v[28:29], v[32:33]
	v_pk_mul_f32 v[30:31], v[30:31], v[34:35]
	v_pk_fma_f32 v[32:33], v[74:75], s[90:91], v[246:247] op_sel_hi:[1,0,1]
	v_pk_fma_f32 v[34:35], v[76:77], s[90:91], v[248:249] op_sel_hi:[1,0,1]
	v_med3_f32 v32, v32, s79, v224
	v_med3_f32 v33, v33, s79, v224
	v_med3_f32 v34, v34, s79, v224
	v_med3_f32 v35, v35, s79, v224
	v_fma_f32 v32, v32, 4.0, 4.0
	v_fma_f32 v33, v33, 4.0, 4.0
	v_fma_f32 v34, v34, 4.0, 4.0
	v_fma_f32 v35, v35, 4.0, 4.0
	v_pk_mul_f32 v[28:29], v[32:33], v[28:29]
	v_pk_mul_f32 v[30:31], v[34:35], v[30:31]
	v_pk_fma_f32 v[36:37], v[70:71], s[90:91], v[242:243] op_sel_hi:[1,0,1]
	v_pk_fma_f32 v[38:39], v[72:73], s[90:91], v[244:245] op_sel_hi:[1,0,1]
	v_min_f32_e32 v36, 0x40e00000, v36
	v_min_f32_e32 v37, 0x40e00000, v37
	v_min_f32_e32 v38, 0x40e00000, v38
	v_min_f32_e32 v39, 0x40e00000, v39
	v_pk_mul_f32 v[32:33], v[36:37], s[92:93] op_sel_hi:[1,0]
	v_pk_mul_f32 v[34:35], v[38:39], s[92:93] op_sel_hi:[1,0]
	v_exp_f32_e32 v32, v32
	v_exp_f32_e32 v33, v33
	v_exp_f32_e32 v34, v34
	v_exp_f32_e32 v35, v35
	v_pk_add_f32 v[32:33], v[32:33], s[96:97] op_sel_hi:[1,0]
	v_pk_add_f32 v[34:35], v[34:35], s[96:97] op_sel_hi:[1,0]
	v_rcp_f32_e32 v32, v32
	v_rcp_f32_e32 v33, v33
	v_rcp_f32_e32 v34, v34
	v_rcp_f32_e32 v35, v35
	v_pk_mul_f32 v[36:37], v[36:37], v[32:33]
	v_pk_mul_f32 v[38:39], v[38:39], v[34:35]
	v_pk_fma_f32 v[32:33], v[66:67], s[90:91], v[250:251] op_sel_hi:[1,0,1]
	v_pk_fma_f32 v[34:35], v[68:69], s[90:91], v[252:253] op_sel_hi:[1,0,1]
	v_med3_f32 v32, v32, s79, v224
	v_med3_f32 v33, v33, s79, v224
	v_med3_f32 v34, v34, s79, v224
	v_med3_f32 v35, v35, s79, v224
	v_fma_f32 v32, v32, 4.0, 4.0
	v_fma_f32 v33, v33, 4.0, 4.0
	v_fma_f32 v34, v34, 4.0, 4.0
	v_fma_f32 v35, v35, 4.0, 4.0
	v_pk_mul_f32 v[36:37], v[32:33], v[36:37]
	v_pk_mul_f32 v[38:39], v[34:35], v[38:39]
	v_add_co_u32_e32 v4, vcc, 0x58000, v18
	s_nop 1
	v_addc_co_u32_e32 v5, vcc, 0, v19, vcc
	s_and_b64 vcc, exec, s[4:5]
	s_mov_b64 s[4:5], -1
	v_mov_b32_e32 v2, v201
	v_mov_b32_e32 v3, v201
	v_cvt_pk_fp8_f32 v2, v28, v29
	v_cvt_pk_fp8_f32 v3, v36, v37
	v_cvt_pk_fp8_f32 v2, v30, v31 op_sel:[0,0,1]
	v_cvt_pk_fp8_f32 v3, v38, v39 op_sel:[0,0,1]
	global_store_dwordx2 v[4:5], v[2:3], off
	s_cbranch_vccnz .LBB0_2061
	s_andn2_b64 vcc, exec, s[20:21]
	s_cbranch_vccnz .LBB0_2060
	s_barrier
	s_branch .LBB0_2060

.LBB0_2154:
	v_lshl_or_b32 v18, s1, 8, v183
	s_ashr_i32 s1, s0, 31
	s_lshl_b64 s[0:1], s[0:1], 13
	s_add_u32 s0, s44, s0
	s_addc_u32 s1, s45, s1
	v_ashrrev_i32_e32 v19, 31, v18
	v_cndmask_b32_e64 v3, 0, 1, s[20:21]
	v_lshl_add_u64 v[20:21], v[18:19], 2, s[0:1]
	v_mov_b32_e32 v2, 0
	v_cmp_ne_u32_e64 s[0:1], 1, v3
	s_andn2_b64 vcc, exec, s[20:21]
	v_mov_b32_e32 v6, 0
	v_mov_b32_e32 v7, 0
	v_mov_b32_e32 v8, 0
	v_mov_b32_e32 v9, 0
	s_nop 15
	s_nop 0
	s_nop 0
	s_nop 0
	s_cbranch_vccnz .LBB0_2156
	v_mov_b32_e32 v6, v238
	v_mov_b32_e32 v7, v239
	v_mov_b32_e32 v8, v240
	v_mov_b32_e32 v9, v241
